# P4 and P6 epilogue stores without nt (h and scores are re-read right after the next barrier), on top of combo2
# speedup vs baseline: 1.0095x; 1.0095x over previous
; __device__ __forceinline__ unsigned cvt_pk_bf16(float lo, float hi) { unsigned r; asm volatile("v_cvt_pk_bf16_f32 %0, %1, %2" : "=v"(r) : "v"(lo), "v"(hi)); return r; }
;     __device__ __forceinline__ void operator()(const f32x4 (&acc)[2][2][4][2], const Unit& u, int wr, int wc, int fr, int fq) const {
;     ...
;             for (int m = 0; m < 4; ++m) { const size_t off = (size_t)(row0 + ai * HALF + m * 16) * ldc + col0;
; #pragma unroll
;                 for (int bj = 0; bj < 2; ++bj) { const f32x4 r0 = __builtin_nontemporal_load((const f32x4*)(R + off + bj * HALF)), r1 = __builtin_nontemporal_load((const f32x4*)(R + off + bj * HALF + 4));
;                     const f32x4 v0 = acc[ai][bj][m][0] + r0, v1 = acc[ai][bj][m][1] + r1;
;                     u32x4 w; w.x = cvt_pk_bf16(v0[0], v0[1]); w.y = cvt_pk_bf16(v0[2], v0[3]); w.z = cvt_pk_bf16(v1[0], v1[1]); w.w = cvt_pk_bf16(v1[2], v1[3]);
;                     __builtin_nontemporal_store(w, (u32x4*)(O + off + bj * HALF)); }
;                 asm volatile("" ::: "memory"); }
.LBB0_566:
	v_lshl_add_u32 v150, s26, 8, v1
	v_lshl_or_b32 v148, s46, 8, v153
	v_lshl_add_u32 v178, v150, 12, v148
	v_lshlrev_b32_e32 v179, 1, v178
	v_lshlrev_b32_e32 v178, 2, v178
	s_andn2_b64 vcc, exec, s[4:5]
	s_mov_b64 s[4:5], -1
	global_load_dwordx4 v[170:173], v178, s[80:81] nt
	global_load_dwordx4 v[174:177], v178, s[80:81] offset:16 nt
	global_load_dwordx4 v[184:187], v178, s[80:81] offset:512 nt
	global_load_dwordx4 v[188:191], v178, s[80:81] offset:528 nt
	v_add_u32_e32 v180, 0x40000, v178
	global_load_dwordx4 v[192:195], v180, s[80:81] nt
	global_load_dwordx4 v[196:199], v180, s[80:81] offset:16 nt
	v_add_u32_e32 v180, 0x40000, v178
	global_load_dwordx4 v[200:203], v180, s[80:81] offset:512 nt
	global_load_dwordx4 v[204:207], v180, s[80:81] offset:528 nt
	v_add_u32_e32 v180, 0x80000, v178
	global_load_dwordx4 v[208:211], v180, s[80:81] nt
	global_load_dwordx4 v[212:215], v180, s[80:81] offset:16 nt
	v_add_u32_e32 v180, 0x80000, v178
	global_load_dwordx4 v[216:219], v180, s[80:81] offset:512 nt
	global_load_dwordx4 v[220:223], v180, s[80:81] offset:528 nt
	v_add_u32_e32 v180, 0xc0000, v178
	global_load_dwordx4 v[224:227], v180, s[80:81] nt
	global_load_dwordx4 v[228:231], v180, s[80:81] offset:16 nt
	v_add_u32_e32 v180, 0xc0000, v178
	global_load_dwordx4 v[232:235], v180, s[80:81] offset:512 nt
	global_load_dwordx4 v[236:239], v180, s[80:81] offset:528 nt
	s_waitcnt vmcnt(14)
	v_pk_add_f32 v[170:171], v[126:127], v[170:171]
	v_pk_add_f32 v[172:173], v[128:129], v[172:173]
	v_pk_add_f32 v[174:175], v[122:123], v[174:175]
	v_pk_add_f32 v[176:177], v[124:125], v[176:177]
	v_cvt_pk_bf16_f32 v122, v170, v171
	v_cvt_pk_bf16_f32 v123, v172, v173
	v_cvt_pk_bf16_f32 v124, v174, v175
	v_cvt_pk_bf16_f32 v125, v176, v177
	global_store_dwordx4 v179, v[122:125], s[6:7]
	v_add_u32_e32 v180, 0x200000, v178
	global_load_dwordx4 v[170:173], v180, s[80:81] nt
	global_load_dwordx4 v[174:177], v180, s[80:81] offset:16 nt
	s_waitcnt vmcnt(15)
	v_pk_add_f32 v[184:185], v[118:119], v[184:185]
	v_pk_add_f32 v[186:187], v[120:121], v[186:187]
	v_pk_add_f32 v[188:189], v[114:115], v[188:189]
	v_pk_add_f32 v[190:191], v[116:117], v[190:191]
	v_cvt_pk_bf16_f32 v114, v184, v185
	v_cvt_pk_bf16_f32 v115, v186, v187
	v_cvt_pk_bf16_f32 v116, v188, v189
	v_cvt_pk_bf16_f32 v117, v190, v191
	global_store_dwordx4 v179, v[114:117], s[6:7] offset:256
	v_add_u32_e32 v180, 0x200000, v178
	global_load_dwordx4 v[184:187], v180, s[80:81] offset:512 nt
	global_load_dwordx4 v[188:191], v180, s[80:81] offset:528 nt
	s_waitcnt vmcnt(16)
	v_pk_add_f32 v[192:193], v[110:111], v[192:193]
	v_pk_add_f32 v[194:195], v[112:113], v[194:195]
	v_pk_add_f32 v[196:197], v[106:107], v[196:197]
	v_pk_add_f32 v[198:199], v[108:109], v[198:199]
	v_cvt_pk_bf16_f32 v106, v192, v193
	v_cvt_pk_bf16_f32 v107, v194, v195
	v_cvt_pk_bf16_f32 v108, v196, v197
	v_cvt_pk_bf16_f32 v109, v198, v199
	v_add_u32_e32 v181, 0x20000, v179
	global_store_dwordx4 v181, v[106:109], s[6:7]
	v_add_u32_e32 v180, 0x240000, v178
	global_load_dwordx4 v[192:195], v180, s[80:81] nt
	global_load_dwordx4 v[196:199], v180, s[80:81] offset:16 nt
	s_waitcnt vmcnt(17)
	v_pk_add_f32 v[200:201], v[102:103], v[200:201]
	v_pk_add_f32 v[202:203], v[104:105], v[202:203]
	v_pk_add_f32 v[204:205], v[98:99], v[204:205]
	v_pk_add_f32 v[206:207], v[100:101], v[206:207]
	v_cvt_pk_bf16_f32 v98, v200, v201
	v_cvt_pk_bf16_f32 v99, v202, v203
	v_cvt_pk_bf16_f32 v100, v204, v205
	v_cvt_pk_bf16_f32 v101, v206, v207
	v_add_u32_e32 v181, 0x20000, v179
	global_store_dwordx4 v181, v[98:101], s[6:7] offset:256
	v_add_u32_e32 v180, 0x240000, v178
	global_load_dwordx4 v[200:203], v180, s[80:81] offset:512 nt
	global_load_dwordx4 v[204:207], v180, s[80:81] offset:528 nt
	s_waitcnt vmcnt(18)
	v_pk_add_f32 v[208:209], v[94:95], v[208:209]
	v_pk_add_f32 v[210:211], v[96:97], v[210:211]
	v_pk_add_f32 v[212:213], v[90:91], v[212:213]
	v_pk_add_f32 v[214:215], v[92:93], v[214:215]
	v_cvt_pk_bf16_f32 v90, v208, v209
	v_cvt_pk_bf16_f32 v91, v210, v211
	v_cvt_pk_bf16_f32 v92, v212, v213
	v_cvt_pk_bf16_f32 v93, v214, v215
	v_add_u32_e32 v181, 0x40000, v179
	global_store_dwordx4 v181, v[90:93], s[6:7]
	v_add_u32_e32 v180, 0x280000, v178
	global_load_dwordx4 v[208:211], v180, s[80:81] nt
	global_load_dwordx4 v[212:215], v180, s[80:81] offset:16 nt
	s_waitcnt vmcnt(19)
	v_pk_add_f32 v[216:217], v[86:87], v[216:217]
	v_pk_add_f32 v[218:219], v[88:89], v[218:219]
	v_pk_add_f32 v[220:221], v[82:83], v[220:221]
	v_pk_add_f32 v[222:223], v[84:85], v[222:223]
	v_cvt_pk_bf16_f32 v82, v216, v217
	v_cvt_pk_bf16_f32 v83, v218, v219
	v_cvt_pk_bf16_f32 v84, v220, v221
	v_cvt_pk_bf16_f32 v85, v222, v223
	v_add_u32_e32 v181, 0x40000, v179
	global_store_dwordx4 v181, v[82:85], s[6:7] offset:256
	v_add_u32_e32 v180, 0x280000, v178
	global_load_dwordx4 v[216:219], v180, s[80:81] offset:512 nt
	global_load_dwordx4 v[220:223], v180, s[80:81] offset:528 nt
	s_waitcnt vmcnt(20)
; __device__ __forceinline__ unsigned cvt_pk_bf16(float lo, float hi) { unsigned r; asm volatile("v_cvt_pk_bf16_f32 %0, %1, %2" : "=v"(r) : "v"(lo), "v"(hi)); return r; }
; #define PG8_BAR __builtin_amdgcn_s_barrier()
;     __device__ __forceinline__ void operator()(const f32x4 (&acc)[2][2][4][2], const Unit& u, int wr, int wc, int fr, int fq) const {
;     ...
;             for (int m = 0; m < 4; ++m) { const size_t off = (size_t)(row0 + ai * HALF + m * 16) * ldc + col0;
; #pragma unroll
;                 for (int bj = 0; bj < 2; ++bj) { const f32x4 r0 = __builtin_nontemporal_load((const f32x4*)(R + off + bj * HALF)), r1 = __builtin_nontemporal_load((const f32x4*)(R + off + bj * HALF + 4));
;                     const f32x4 v0 = acc[ai][bj][m][0] + r0, v1 = acc[ai][bj][m][1] + r1;
;                     u32x4 w; w.x = cvt_pk_bf16(v0[0], v0[1]); w.y = cvt_pk_bf16(v0[2], v0[3]); w.z = cvt_pk_bf16(v1[0], v1[1]); w.w = cvt_pk_bf16(v1[2], v1[3]);
;                     __builtin_nontemporal_store(w, (u32x4*)(O + off + bj * HALF)); }
;                 asm volatile("" ::: "memory"); }
; template <class Epi, class Sched, bool ALIGN_EPI = false, bool SP2 = false>
; __device__ __forceinline__ void gemm_phase(PG8_LAS unsigned char* lds, const Gemm g, const Sched& S, const Epi& E) {
;     ...
;         if constexpr (ALIGN_EPI) { if (wr == 0) PG8_BAR; }
;         if constexpr (!Epi::AFTER_DRAIN) { E(acc, cur, wr, wc, fr, fq); S.done(cur); }
;         if (!has_next) break;
; #pragma unroll
;         for (int a = 0; a < 2; ++a)
; #pragma unroll
;             for (int b = 0; b < 2; ++b)
; #pragma unroll
;                 for (int m = 0; m < 4; ++m)
; #pragma unroll
;                     for (int n = 0; n < 2; ++n) acc[a][b][m][n] = (f32x4){0.f, 0.f, 0.f, 0.f};
;         cur = nxt; cA = nA; cB = nB; ++ui;
;         if constexpr (ALIGN_EPI) { if (wr == 1) PG8_BAR; }
	v_pk_add_f32 v[224:225], v[78:79], v[224:225]
	v_pk_add_f32 v[226:227], v[80:81], v[226:227]
	v_pk_add_f32 v[228:229], v[74:75], v[228:229]
	v_pk_add_f32 v[230:231], v[76:77], v[230:231]
	v_cvt_pk_bf16_f32 v74, v224, v225
	v_cvt_pk_bf16_f32 v75, v226, v227
	v_cvt_pk_bf16_f32 v76, v228, v229
	v_cvt_pk_bf16_f32 v77, v230, v231
	v_add_u32_e32 v181, 0x60000, v179
	global_store_dwordx4 v181, v[74:77], s[6:7]
	v_add_u32_e32 v180, 0x2c0000, v178
	global_load_dwordx4 v[224:227], v180, s[80:81] nt
	global_load_dwordx4 v[228:231], v180, s[80:81] offset:16 nt
	s_waitcnt vmcnt(21)
	v_pk_add_f32 v[232:233], v[70:71], v[232:233]
	v_pk_add_f32 v[234:235], v[72:73], v[234:235]
	v_pk_add_f32 v[236:237], v[66:67], v[236:237]
	v_pk_add_f32 v[238:239], v[68:69], v[238:239]
	v_cvt_pk_bf16_f32 v66, v232, v233
	v_cvt_pk_bf16_f32 v67, v234, v235
	v_cvt_pk_bf16_f32 v68, v236, v237
	v_cvt_pk_bf16_f32 v69, v238, v239
	v_add_u32_e32 v181, 0x60000, v179
	global_store_dwordx4 v181, v[66:69], s[6:7] offset:256
	v_add_u32_e32 v180, 0x2c0000, v178
	global_load_dwordx4 v[232:235], v180, s[80:81] offset:512 nt
	global_load_dwordx4 v[236:239], v180, s[80:81] offset:528 nt
	s_waitcnt vmcnt(21)
	v_pk_add_f32 v[170:171], v[62:63], v[170:171]
	v_pk_add_f32 v[172:173], v[64:65], v[172:173]
	v_pk_add_f32 v[174:175], v[58:59], v[174:175]
	v_pk_add_f32 v[176:177], v[60:61], v[176:177]
	v_cvt_pk_bf16_f32 v58, v170, v171
	v_cvt_pk_bf16_f32 v59, v172, v173
	v_cvt_pk_bf16_f32 v60, v174, v175
	v_cvt_pk_bf16_f32 v61, v176, v177
	v_add_u32_e32 v181, 0x100000, v179
	global_store_dwordx4 v181, v[58:61], s[6:7]
	s_waitcnt vmcnt(19)
	v_pk_add_f32 v[184:185], v[54:55], v[184:185]
	v_pk_add_f32 v[186:187], v[56:57], v[186:187]
	v_pk_add_f32 v[188:189], v[50:51], v[188:189]
	v_pk_add_f32 v[190:191], v[52:53], v[190:191]
	v_cvt_pk_bf16_f32 v50, v184, v185
	v_cvt_pk_bf16_f32 v51, v186, v187
	v_cvt_pk_bf16_f32 v52, v188, v189
	v_cvt_pk_bf16_f32 v53, v190, v191
	v_add_u32_e32 v181, 0x100000, v179
	global_store_dwordx4 v181, v[50:53], s[6:7] offset:256
	s_waitcnt vmcnt(17)
	v_pk_add_f32 v[192:193], v[46:47], v[192:193]
	v_pk_add_f32 v[194:195], v[48:49], v[194:195]
	v_pk_add_f32 v[196:197], v[42:43], v[196:197]
	v_pk_add_f32 v[198:199], v[44:45], v[198:199]
	v_cvt_pk_bf16_f32 v42, v192, v193
	v_cvt_pk_bf16_f32 v43, v194, v195
	v_cvt_pk_bf16_f32 v44, v196, v197
	v_cvt_pk_bf16_f32 v45, v198, v199
	v_add_u32_e32 v181, 0x120000, v179
	global_store_dwordx4 v181, v[42:45], s[6:7]
	s_waitcnt vmcnt(15)
	v_pk_add_f32 v[200:201], v[38:39], v[200:201]
	v_pk_add_f32 v[202:203], v[40:41], v[202:203]
	v_pk_add_f32 v[204:205], v[34:35], v[204:205]
	v_pk_add_f32 v[206:207], v[36:37], v[206:207]
	v_cvt_pk_bf16_f32 v34, v200, v201
	v_cvt_pk_bf16_f32 v35, v202, v203
	v_cvt_pk_bf16_f32 v36, v204, v205
	v_cvt_pk_bf16_f32 v37, v206, v207
	v_add_u32_e32 v181, 0x120000, v179
	global_store_dwordx4 v181, v[34:37], s[6:7] offset:256
	s_waitcnt vmcnt(13)
	v_pk_add_f32 v[208:209], v[30:31], v[208:209]
	v_pk_add_f32 v[210:211], v[32:33], v[210:211]
	v_pk_add_f32 v[212:213], v[26:27], v[212:213]
	v_pk_add_f32 v[214:215], v[28:29], v[214:215]
	v_cvt_pk_bf16_f32 v26, v208, v209
	v_cvt_pk_bf16_f32 v27, v210, v211
	v_cvt_pk_bf16_f32 v28, v212, v213
	v_cvt_pk_bf16_f32 v29, v214, v215
	v_add_u32_e32 v181, 0x140000, v179
	global_store_dwordx4 v181, v[26:29], s[6:7]
	s_waitcnt vmcnt(11)
	v_pk_add_f32 v[216:217], v[22:23], v[216:217]
	v_pk_add_f32 v[218:219], v[24:25], v[218:219]
	v_pk_add_f32 v[220:221], v[18:19], v[220:221]
	v_pk_add_f32 v[222:223], v[20:21], v[222:223]
	v_cvt_pk_bf16_f32 v18, v216, v217
	v_cvt_pk_bf16_f32 v19, v218, v219
	v_cvt_pk_bf16_f32 v20, v220, v221
	v_cvt_pk_bf16_f32 v21, v222, v223
	v_add_u32_e32 v181, 0x140000, v179
	global_store_dwordx4 v181, v[18:21], s[6:7] offset:256
	s_waitcnt vmcnt(9)
	v_pk_add_f32 v[224:225], v[14:15], v[224:225]
	v_pk_add_f32 v[226:227], v[16:17], v[226:227]
	v_pk_add_f32 v[228:229], v[10:11], v[228:229]
	v_pk_add_f32 v[230:231], v[12:13], v[230:231]
	v_cvt_pk_bf16_f32 v10, v224, v225
	v_cvt_pk_bf16_f32 v11, v226, v227
	v_cvt_pk_bf16_f32 v12, v228, v229
	v_cvt_pk_bf16_f32 v13, v230, v231
	v_add_u32_e32 v181, 0x160000, v179
	global_store_dwordx4 v181, v[10:13], s[6:7]
	s_waitcnt vmcnt(7)
	v_pk_add_f32 v[232:233], v[6:7], v[232:233]
	v_pk_add_f32 v[234:235], v[8:9], v[234:235]
	v_pk_add_f32 v[236:237], v[2:3], v[236:237]
	v_pk_add_f32 v[238:239], v[4:5], v[238:239]
	v_cvt_pk_bf16_f32 v2, v232, v233
	v_cvt_pk_bf16_f32 v3, v234, v235
	v_cvt_pk_bf16_f32 v4, v236, v237
	v_cvt_pk_bf16_f32 v5, v238, v239
	v_add_u32_e32 v181, 0x160000, v179
	global_store_dwordx4 v181, v[2:5], s[6:7] offset:256
	s_cbranch_vccnz .LBB0_555
	s_andn2_b64 vcc, exec, s[0:1]
	s_cbranch_vccnz .LBB0_554
	s_barrier
	s_branch .LBB0_554

;     __device__ __forceinline__ void operator()(const f32x4 (&acc)[2][2][4][2], const Unit& u, int wr, int wc, int fr, int fq) const {
;         const int row0 = u.pm * BM + wr * 64 + fr, col0 = u.pn * BM + wc * 32 + 4 * fq;
; #pragma unroll
;         for (int ai = 0; ai < 2; ++ai)
; #pragma unroll
;             for (int m = 0; m < 4; ++m) { const int row = row0 + ai * HALF + m * 16; const float rsv = rowscale[row]; const size_t off = (size_t)row * ldc + col0;
; #pragma unroll
;                 for (int bj = 0; bj < 2; ++bj)
; #pragma unroll
;                     for (int n = 0; n < 2; ++n) __builtin_nontemporal_store(acc[ai][bj][m][n] * rsv, (f32x4*)(C + off + bj * HALF + n * 16)); }
.LBB0_710:
	v_lshl_add_u32 v154, s0, 8, v148
	v_ashrrev_i32_e32 v155, 31, v154
	v_lshl_add_u64 v[142:143], v[154:155], 2, s[10:11]
	global_load_dword v184, v[142:143], off
	global_load_dword v186, v[142:143], off offset:64
	global_load_dword v188, v[142:143], off offset:128
	global_load_dword v190, v[142:143], off offset:192
	global_load_dword v192, v[142:143], off offset:512
	global_load_dword v194, v[142:143], off offset:576
	global_load_dword v196, v[142:143], off offset:640
	global_load_dword v198, v[142:143], off offset:704
	v_lshl_or_b32 v144, s1, 8, v150
	v_ashrrev_i32_e32 v145, 31, v144
	v_lshlrev_b64 v[160:161], 13, v[154:155]
	v_or_b32_e32 v158, 16, v154
	v_lshlrev_b64 v[162:163], 2, v[144:145]
	v_lshl_add_u64 v[144:145], s[40:41], 0, v[160:161]
	v_ashrrev_i32_e32 v159, 31, v158
	v_lshl_add_u64 v[144:145], v[144:145], 0, v[162:163]
	v_lshl_add_u64 v[160:161], v[158:159], 2, s[10:11]
	s_waitcnt vmcnt(0)
	v_pk_mul_f32 v[128:129], v[128:129], v[184:185] op_sel_hi:[1,0]
	v_pk_mul_f32 v[126:127], v[126:127], v[184:185] op_sel_hi:[1,0]
	v_pk_mul_f32 v[124:125], v[124:125], v[184:185] op_sel_hi:[1,0]
	v_pk_mul_f32 v[122:123], v[122:123], v[184:185] op_sel_hi:[1,0]
	v_pk_mul_f32 v[120:121], v[120:121], v[184:185] op_sel_hi:[1,0]
	v_pk_mul_f32 v[118:119], v[118:119], v[184:185] op_sel_hi:[1,0]
	v_pk_mul_f32 v[116:117], v[116:117], v[184:185] op_sel_hi:[1,0]
	v_pk_mul_f32 v[114:115], v[114:115], v[184:185] op_sel_hi:[1,0]
	global_store_dwordx4 v[144:145], v[126:129], off
	global_store_dwordx4 v[144:145], v[122:125], off offset:64
	global_store_dwordx4 v[144:145], v[118:121], off offset:512
	global_store_dwordx4 v[144:145], v[114:117], off offset:576
	s_nop 3
	v_lshlrev_b64 v[118:119], 13, v[158:159]
	v_or_b32_e32 v116, 32, v154
	v_lshl_add_u64 v[118:119], s[40:41], 0, v[118:119]
	v_ashrrev_i32_e32 v117, 31, v116
	v_lshl_add_u64 v[118:119], v[118:119], 0, v[162:163]
	v_lshl_add_u64 v[120:121], v[116:117], 2, s[10:11]
	s_nop 3
	v_pk_mul_f32 v[112:113], v[112:113], v[186:187] op_sel_hi:[1,0]
	v_pk_mul_f32 v[110:111], v[110:111], v[186:187] op_sel_hi:[1,0]
	v_pk_mul_f32 v[108:109], v[108:109], v[186:187] op_sel_hi:[1,0]
	v_pk_mul_f32 v[106:107], v[106:107], v[186:187] op_sel_hi:[1,0]
	v_pk_mul_f32 v[104:105], v[104:105], v[186:187] op_sel_hi:[1,0]
	v_pk_mul_f32 v[102:103], v[102:103], v[186:187] op_sel_hi:[1,0]
	v_pk_mul_f32 v[100:101], v[100:101], v[186:187] op_sel_hi:[1,0]
	v_pk_mul_f32 v[98:99], v[98:99], v[186:187] op_sel_hi:[1,0]
	global_store_dwordx4 v[118:119], v[110:113], off
	global_store_dwordx4 v[118:119], v[106:109], off offset:64
	global_store_dwordx4 v[118:119], v[102:105], off offset:512
	global_store_dwordx4 v[118:119], v[98:101], off offset:576
	s_nop 3
	v_lshlrev_b64 v[102:103], 13, v[116:117]
	v_or_b32_e32 v100, 48, v154
	v_lshl_add_u64 v[102:103], s[40:41], 0, v[102:103]
	v_ashrrev_i32_e32 v101, 31, v100
	v_lshl_add_u64 v[102:103], v[102:103], 0, v[162:163]
	v_lshl_add_u64 v[104:105], v[100:101], 2, s[10:11]
	s_nop 3
	v_pk_mul_f32 v[96:97], v[96:97], v[188:189] op_sel_hi:[1,0]
	v_pk_mul_f32 v[94:95], v[94:95], v[188:189] op_sel_hi:[1,0]
	v_pk_mul_f32 v[92:93], v[92:93], v[188:189] op_sel_hi:[1,0]
	v_pk_mul_f32 v[90:91], v[90:91], v[188:189] op_sel_hi:[1,0]
	v_pk_mul_f32 v[84:85], v[84:85], v[188:189] op_sel_hi:[1,0]
	v_pk_mul_f32 v[82:83], v[82:83], v[188:189] op_sel_hi:[1,0]
	v_pk_mul_f32 v[76:77], v[76:77], v[188:189] op_sel_hi:[1,0]
	v_pk_mul_f32 v[74:75], v[74:75], v[188:189] op_sel_hi:[1,0]
	global_store_dwordx4 v[102:103], v[94:97], off
	global_store_dwordx4 v[102:103], v[90:93], off offset:64
	global_store_dwordx4 v[102:103], v[82:85], off offset:512
	global_store_dwordx4 v[102:103], v[74:77], off offset:576
	s_nop 3
	s_nop 3
	v_pk_mul_f32 v[80:81], v[80:81], v[190:191] op_sel_hi:[1,0]
	v_lshlrev_b64 v[74:75], 13, v[100:101]
	v_lshl_add_u64 v[74:75], s[40:41], 0, v[74:75]
	v_lshl_add_u64 v[84:85], v[74:75], 0, v[162:163]
	v_pk_mul_f32 v[76:77], v[88:89], v[190:191] op_sel_hi:[1,0]
	v_pk_mul_f32 v[74:75], v[86:87], v[190:191] op_sel_hi:[1,0]
	v_pk_mul_f32 v[78:79], v[78:79], v[190:191] op_sel_hi:[1,0]
; #define PG8_BAR __builtin_amdgcn_s_barrier()
;     __device__ __forceinline__ void operator()(const f32x4 (&acc)[2][2][4][2], const Unit& u, int wr, int wc, int fr, int fq) const {
;         const int row0 = u.pm * BM + wr * 64 + fr, col0 = u.pn * BM + wc * 32 + 4 * fq;
; #pragma unroll
;         for (int ai = 0; ai < 2; ++ai)
; #pragma unroll
;             for (int m = 0; m < 4; ++m) { const int row = row0 + ai * HALF + m * 16; const float rsv = rowscale[row]; const size_t off = (size_t)row * ldc + col0;
; #pragma unroll
;                 for (int bj = 0; bj < 2; ++bj)
; #pragma unroll
;                     for (int n = 0; n < 2; ++n) __builtin_nontemporal_store(acc[ai][bj][m][n] * rsv, (f32x4*)(C + off + bj * HALF + n * 16)); }
; template <class Epi, class Sched, bool ALIGN_EPI = false, bool SP2 = false>
; __device__ __forceinline__ void gemm_phase(PG8_LAS unsigned char* lds, const Gemm g, const Sched& S, const Epi& E) {
;     ...
;         if constexpr (ALIGN_EPI) { if (wr == 0) PG8_BAR; }
;         if constexpr (!Epi::AFTER_DRAIN) { E(acc, cur, wr, wc, fr, fq); S.done(cur); }
;         if (!has_next) break;
; #pragma unroll
;         for (int a = 0; a < 2; ++a)
; #pragma unroll
;             for (int b = 0; b < 2; ++b)
; #pragma unroll
;                 for (int m = 0; m < 4; ++m)
; #pragma unroll
;                     for (int n = 0; n < 2; ++n) acc[a][b][m][n] = (f32x4){0.f, 0.f, 0.f, 0.f};
;         cur = nxt; cA = nA; cB = nB; ++ui;
;         if constexpr (ALIGN_EPI) { if (wr == 1) PG8_BAR; }
	v_pk_mul_f32 v[72:73], v[72:73], v[190:191] op_sel_hi:[1,0]
	v_pk_mul_f32 v[70:71], v[70:71], v[190:191] op_sel_hi:[1,0]
	v_pk_mul_f32 v[68:69], v[68:69], v[190:191] op_sel_hi:[1,0]
	v_pk_mul_f32 v[66:67], v[66:67], v[190:191] op_sel_hi:[1,0]
	global_store_dwordx4 v[84:85], v[74:77], off
	global_store_dwordx4 v[84:85], v[78:81], off offset:64
	global_store_dwordx4 v[84:85], v[70:73], off offset:512
	global_store_dwordx4 v[84:85], v[66:69], off offset:576
	s_nop 3
	v_add_co_u32_e32 v70, vcc, s53, v144
	v_lshl_add_u64 v[68:69], v[144:145], 0, s[2:3]
	s_nop 0
	v_addc_co_u32_e32 v71, vcc, 0, v145, vcc
	s_nop 3
	v_pk_mul_f32 v[64:65], v[64:65], v[192:193] op_sel_hi:[1,0]
	v_pk_mul_f32 v[62:63], v[62:63], v[192:193] op_sel_hi:[1,0]
	v_pk_mul_f32 v[60:61], v[60:61], v[192:193] op_sel_hi:[1,0]
	v_pk_mul_f32 v[58:59], v[58:59], v[192:193] op_sel_hi:[1,0]
	v_pk_mul_f32 v[56:57], v[56:57], v[192:193] op_sel_hi:[1,0]
	v_pk_mul_f32 v[54:55], v[54:55], v[192:193] op_sel_hi:[1,0]
	v_pk_mul_f32 v[48:49], v[48:49], v[192:193] op_sel_hi:[1,0]
	v_pk_mul_f32 v[46:47], v[46:47], v[192:193] op_sel_hi:[1,0]
	global_store_dwordx4 v[70:71], v[62:65], off
	global_store_dwordx4 v[68:69], v[58:61], off offset:64
	global_store_dwordx4 v[68:69], v[54:57], off offset:512
	global_store_dwordx4 v[68:69], v[46:49], off offset:576
	s_nop 3
	v_add_co_u32_e32 v58, vcc, s54, v144
	v_lshl_add_u64 v[56:57], v[144:145], 0, s[16:17]
	s_nop 0
	v_addc_co_u32_e32 v59, vcc, 0, v145, vcc
	s_nop 3
	v_pk_mul_f32 v[48:49], v[52:53], v[194:195] op_sel_hi:[1,0]
	v_pk_mul_f32 v[46:47], v[50:51], v[194:195] op_sel_hi:[1,0]
	v_pk_mul_f32 v[44:45], v[44:45], v[194:195] op_sel_hi:[1,0]
	v_pk_mul_f32 v[42:43], v[42:43], v[194:195] op_sel_hi:[1,0]
	v_pk_mul_f32 v[40:41], v[40:41], v[194:195] op_sel_hi:[1,0]
	v_pk_mul_f32 v[38:39], v[38:39], v[194:195] op_sel_hi:[1,0]
	v_pk_mul_f32 v[32:33], v[32:33], v[194:195] op_sel_hi:[1,0]
	v_pk_mul_f32 v[30:31], v[30:31], v[194:195] op_sel_hi:[1,0]
	global_store_dwordx4 v[58:59], v[46:49], off
	global_store_dwordx4 v[56:57], v[42:45], off offset:64
	global_store_dwordx4 v[56:57], v[38:41], off offset:512
	global_store_dwordx4 v[56:57], v[30:33], off offset:576
	s_nop 3
	v_add_co_u32_e32 v42, vcc, s55, v144
	v_lshl_add_u64 v[40:41], v[144:145], 0, s[18:19]
	s_nop 0
	v_addc_co_u32_e32 v43, vcc, 0, v145, vcc
	s_andn2_b64 vcc, exec, s[4:5]
	s_nop 3
	v_pk_mul_f32 v[32:33], v[36:37], v[196:197] op_sel_hi:[1,0]
	v_pk_mul_f32 v[30:31], v[34:35], v[196:197] op_sel_hi:[1,0]
	v_pk_mul_f32 v[28:29], v[28:29], v[196:197] op_sel_hi:[1,0]
	v_pk_mul_f32 v[26:27], v[26:27], v[196:197] op_sel_hi:[1,0]
	v_pk_mul_f32 v[24:25], v[24:25], v[196:197] op_sel_hi:[1,0]
	v_pk_mul_f32 v[22:23], v[22:23], v[196:197] op_sel_hi:[1,0]
	v_pk_mul_f32 v[20:21], v[20:21], v[196:197] op_sel_hi:[1,0]
	v_pk_mul_f32 v[18:19], v[18:19], v[196:197] op_sel_hi:[1,0]
	global_store_dwordx4 v[42:43], v[30:33], off
	global_store_dwordx4 v[40:41], v[26:29], off offset:64
	global_store_dwordx4 v[40:41], v[22:25], off offset:512
	global_store_dwordx4 v[40:41], v[18:21], off offset:576
	s_nop 3
	v_add_co_u32_e64 v22, s[0:1], s56, v144
	v_lshl_add_u64 v[20:21], v[144:145], 0, s[20:21]
	s_nop 0
	v_addc_co_u32_e64 v23, s[0:1], 0, v145, s[0:1]
	s_mov_b64 s[0:1], -1
	s_nop 3
	v_pk_mul_f32 v[16:17], v[16:17], v[198:199] op_sel_hi:[1,0]
	v_pk_mul_f32 v[14:15], v[14:15], v[198:199] op_sel_hi:[1,0]
	v_pk_mul_f32 v[12:13], v[12:13], v[198:199] op_sel_hi:[1,0]
	v_pk_mul_f32 v[10:11], v[10:11], v[198:199] op_sel_hi:[1,0]
	v_pk_mul_f32 v[8:9], v[8:9], v[198:199] op_sel_hi:[1,0]
	v_pk_mul_f32 v[6:7], v[6:7], v[198:199] op_sel_hi:[1,0]
	v_pk_mul_f32 v[4:5], v[4:5], v[198:199] op_sel_hi:[1,0]
	v_pk_mul_f32 v[2:3], v[2:3], v[198:199] op_sel_hi:[1,0]
	global_store_dwordx4 v[22:23], v[14:17], off
	global_store_dwordx4 v[20:21], v[10:13], off offset:64
	global_store_dwordx4 v[20:21], v[6:9], off offset:512
	global_store_dwordx4 v[20:21], v[2:5], off offset:576
	s_cbranch_vccnz .LBB0_699
	s_andn2_b64 vcc, exec, s[8:9]
	s_cbranch_vccnz .LBB0_698
	s_barrier
	s_branch .LBB0_698
